# GEMM_OUT unit-loop header no longer drains epilogue stores; ROW_MIX layer0 prefetch wait moved to latch end (on top of mixer counted waits)
# speedup vs baseline: 1.0127x; 1.0011x over previous
.LBB0_557:
	s_ashr_i32 s27, s26, 31
	s_lshl_b64 s[28:29], s[26:27], 19
	s_add_u32 s28, s49, s28
	s_addc_u32 s29, s50, s29
	s_ashr_i32 s25, s24, 31
	s_lshl_b64 s[30:31], s[24:25], 19
	s_add_u32 s30, s47, s30
	s_addc_u32 s31, s48, s31
	s_and_b64 s[38:39], s[8:9], exec
	v_mov_b32_e32 v0, 0
	s_cselect_b32 s1, s31, s35
	s_cselect_b32 s3, s30, s34
	s_mov_b32 s20, -2
	s_mov_b64 s[38:39], 0
	s_waitcnt lgkmcnt(0)
	v_mov_b32_e32 v1, v0
	v_mov_b32_e32 v2, v0
	v_mov_b32_e32 v3, v0
	v_mov_b32_e32 v4, v0
	v_mov_b32_e32 v5, v0
	v_mov_b32_e32 v6, v0
	v_mov_b32_e32 v7, v0
	v_mov_b32_e32 v16, v0
	v_mov_b32_e32 v17, v0
	v_mov_b32_e32 v18, v0
	v_mov_b32_e32 v19, v0
	v_mov_b32_e32 v20, v0
	v_mov_b32_e32 v21, v0
	v_mov_b32_e32 v22, v0
	v_mov_b32_e32 v23, v0
	v_mov_b32_e32 v32, v0
	v_mov_b32_e32 v33, v0
	v_mov_b32_e32 v34, v0
	v_mov_b32_e32 v35, v0
	v_mov_b32_e32 v36, v0
	v_mov_b32_e32 v37, v0
	v_mov_b32_e32 v38, v0
	v_mov_b32_e32 v39, v0
	v_mov_b32_e32 v48, v0
	v_mov_b32_e32 v49, v0
	v_mov_b32_e32 v50, v0
	v_mov_b32_e32 v51, v0
	v_mov_b64_e32 v[8:9], 0
	v_mov_b64_e32 v[10:11], 0
	v_mov_b64_e32 v[12:13], 0
	v_mov_b64_e32 v[14:15], 0
	v_mov_b64_e32 v[24:25], 0
	v_mov_b64_e32 v[26:27], 0
	v_mov_b64_e32 v[28:29], 0
	v_mov_b64_e32 v[30:31], 0
	v_mov_b64_e32 v[40:41], 0
	v_mov_b64_e32 v[42:43], 0
	v_mov_b64_e32 v[44:45], 0
	v_mov_b64_e32 v[46:47], 0
	v_mov_b64_e32 v[52:53], 0
	v_mov_b64_e32 v[54:55], 0
	v_mov_b64_e32 v[56:57], 0
	v_mov_b64_e32 v[58:59], 0
	v_mov_b64_e32 v[60:61], 0
	v_mov_b64_e32 v[62:63], 0
	v_mov_b64_e32 v[64:65], 0
	v_mov_b64_e32 v[66:67], 0
	v_mov_b64_e32 v[68:69], 0
	v_mov_b64_e32 v[70:71], 0
	v_mov_b64_e32 v[72:73], 0
	v_mov_b64_e32 v[74:75], 0
	v_mov_b64_e32 v[76:77], 0
	v_mov_b64_e32 v[78:79], 0
	v_mov_b64_e32 v[80:81], 0
	v_mov_b64_e32 v[82:83], 0
	v_mov_b64_e32 v[84:85], 0
	v_mov_b64_e32 v[86:87], 0
	v_mov_b64_e32 v[96:97], 0
	v_mov_b64_e32 v[98:99], 0
	v_mov_b64_e32 v[100:101], 0
	v_mov_b64_e32 v[102:103], 0
	v_mov_b64_e32 v[112:113], 0
	v_mov_b64_e32 v[114:115], 0
	v_mov_b64_e32 v[116:117], 0
	v_mov_b64_e32 v[118:119], 0
	v_mov_b64_e32 v[120:121], 0
	v_mov_b64_e32 v[122:123], 0
	v_mov_b64_e32 v[124:125], 0
	v_mov_b64_e32 v[126:127], 0
	v_mov_b64_e32 v[128:129], 0
	v_mov_b64_e32 v[130:131], 0
	v_mov_b64_e32 v[132:133], 0
	v_mov_b64_e32 v[134:135], 0
	v_mov_b64_e32 v[136:137], 0
	v_mov_b64_e32 v[138:139], 0
	v_mov_b64_e32 v[140:141], 0
	v_mov_b64_e32 v[142:143], 0
.LBB0_558:
	s_add_u32 s40, s38, 0x100
	ds_read_b128 v[88:91], v163
	ds_read_b128 v[92:95], v164
	ds_read_b128 v[104:107], v171
	ds_read_b128 v[108:111], v172
	s_addc_u32 s41, s39, 0
	s_and_b32 s25, s40, 0x700
	s_add_u32 s27, s34, s25
	s_addc_u32 s33, s35, 0
	s_cmp_eq_u32 s20, 12
	s_cselect_b64 s[44:45], -1, 0
	s_and_b64 s[42:43], s[44:45], exec
	s_cselect_b32 s43, s1, s33
	s_cselect_b32 s42, s3, s27
	s_cselect_b32 s27, 0, 0
	s_cselect_b32 s25, 0, s25
	s_add_u32 s33, s36, s38
	s_addc_u32 s39, s37, s39
	s_add_u32 s38, s33, 0x40080
	s_addc_u32 s39, s39, 0
	ds_read_b128 v[158:161], v179
	ds_read_b128 v[180:183], v179 offset:1024
	ds_read_b128 v[184:187], v179 offset:2048
	ds_read_b128 v[188:191], v179 offset:3072
	ds_read_b128 v[192:195], v179 offset:4096
	ds_read_b128 v[196:199], v179 offset:5120
	ds_read_b128 v[200:203], v179 offset:6144
	ds_read_b128 v[204:207], v179 offset:7168
	s_add_i32 m0, s51, 0xc000
	s_nop 0
	global_load_lds_dwordx4 v144, s[38:39]
	s_add_i32 m0, s51, 0xe000
	s_nop 0
	global_load_lds_dwordx4 v148, s[38:39]
	s_waitcnt lgkmcnt(8)
	s_barrier
	s_waitcnt lgkmcnt(0)
	s_setprio 1
	s_waitcnt lgkmcnt(0)
	v_mfma_f32_16x16x32_bf16 v[140:143], v[88:91], v[158:161], v[140:143]
	v_mfma_f32_16x16x32_bf16 v[136:139], v[104:107], v[158:161], v[136:139]
	v_mfma_f32_16x16x32_bf16 v[124:127], v[88:91], v[184:187], v[124:127]
	v_mfma_f32_16x16x32_bf16 v[120:123], v[104:107], v[184:187], v[120:123]
	v_mfma_f32_16x16x32_bf16 v[100:103], v[88:91], v[192:195], v[100:103]
	v_mfma_f32_16x16x32_bf16 v[96:99], v[104:107], v[192:195], v[96:99]
	v_mfma_f32_16x16x32_bf16 v[76:79], v[88:91], v[200:203], v[76:79]
	v_mfma_f32_16x16x32_bf16 v[72:75], v[104:107], v[200:203], v[72:75]
	v_mfma_f32_16x16x32_bf16 v[140:143], v[92:95], v[180:183], v[140:143]
	v_mfma_f32_16x16x32_bf16 v[136:139], v[108:111], v[180:183], v[136:139]
	v_mfma_f32_16x16x32_bf16 v[124:127], v[92:95], v[188:191], v[124:127]
	v_mfma_f32_16x16x32_bf16 v[120:123], v[108:111], v[188:191], v[120:123]
	v_mfma_f32_16x16x32_bf16 v[100:103], v[92:95], v[196:199], v[100:103]
	v_mfma_f32_16x16x32_bf16 v[96:99], v[108:111], v[196:199], v[96:99]
	v_mfma_f32_16x16x32_bf16 v[76:79], v[92:95], v[204:207], v[76:79]
	v_mfma_f32_16x16x32_bf16 v[72:75], v[108:111], v[204:207], v[72:75]
	s_setprio 0
	s_barrier
	s_mov_b64 s[38:39], s[42:43]
	s_mov_b32 m0, s52
	ds_read_b128 v[210:213], v165
	ds_read_b128 v[214:217], v166
	ds_read_b128 v[218:221], v173
	ds_read_b128 v[222:225], v174
	s_nop 0
	global_load_lds_dwordx4 v146, s[38:39]
	s_mov_b32 m0, s53
	s_nop 0
	global_load_lds_dwordx4 v150, s[38:39]
	s_nop 0
	s_barrier
	s_waitcnt lgkmcnt(0)
	s_setprio 1
	s_waitcnt lgkmcnt(0)
	v_mfma_f32_16x16x32_bf16 v[132:135], v[210:213], v[158:161], v[132:135]
	v_mfma_f32_16x16x32_bf16 v[128:131], v[218:221], v[158:161], v[128:131]
	v_mfma_f32_16x16x32_bf16 v[116:119], v[210:213], v[184:187], v[116:119]
	v_mfma_f32_16x16x32_bf16 v[112:115], v[218:221], v[184:187], v[112:115]
	v_mfma_f32_16x16x32_bf16 v[84:87], v[210:213], v[192:195], v[84:87]
	v_mfma_f32_16x16x32_bf16 v[80:83], v[218:221], v[192:195], v[80:83]
	v_mfma_f32_16x16x32_bf16 v[68:71], v[210:213], v[200:203], v[68:71]
	v_mfma_f32_16x16x32_bf16 v[64:67], v[218:221], v[200:203], v[64:67]
	v_mfma_f32_16x16x32_bf16 v[132:135], v[214:217], v[180:183], v[132:135]
	v_mfma_f32_16x16x32_bf16 v[128:131], v[222:225], v[180:183], v[128:131]
	v_mfma_f32_16x16x32_bf16 v[116:119], v[214:217], v[188:191], v[116:119]
	v_mfma_f32_16x16x32_bf16 v[112:115], v[222:225], v[188:191], v[112:115]
	v_mfma_f32_16x16x32_bf16 v[84:87], v[214:217], v[196:199], v[84:87]
	v_mfma_f32_16x16x32_bf16 v[80:83], v[222:225], v[196:199], v[80:83]
	v_mfma_f32_16x16x32_bf16 v[68:71], v[214:217], v[204:207], v[68:71]
	v_mfma_f32_16x16x32_bf16 v[64:67], v[222:225], v[204:207], v[64:67]
	s_setprio 0
	s_and_b64 s[38:39], s[8:9], s[44:45]
	s_and_b64 s[38:39], s[38:39], exec
	s_cselect_b32 s38, s28, s36
	s_cselect_b32 s33, s29, s37
	s_add_u32 s38, s38, s25
	s_addc_u32 s39, s33, s27
	s_mov_b64 s[44:45], s[38:39]
	s_mov_b32 m0, s51
	s_barrier
	ds_read_b128 v[158:161], v179 offset:16384
	ds_read_b128 v[180:183], v179 offset:17408
	ds_read_b128 v[184:187], v179 offset:18432
	ds_read_b128 v[188:191], v179 offset:19456
	ds_read_b128 v[192:195], v179 offset:20480
	ds_read_b128 v[196:199], v179 offset:21504
	ds_read_b128 v[200:203], v179 offset:22528
	ds_read_b128 v[204:207], v179 offset:23552
	s_nop 0
	global_load_lds_dwordx4 v144, s[44:45]
	s_mov_b32 m0, s54
	s_nop 0
	global_load_lds_dwordx4 v148, s[44:45]
	s_nop 0
	s_barrier
	s_waitcnt lgkmcnt(0)
	s_setprio 1
	s_waitcnt lgkmcnt(0)
	v_mfma_f32_16x16x32_bf16 v[60:63], v[88:91], v[158:161], v[60:63]
	v_mfma_f32_16x16x32_bf16 v[56:59], v[104:107], v[158:161], v[56:59]
	v_mfma_f32_16x16x32_bf16 v[44:47], v[88:91], v[184:187], v[44:47]
	v_mfma_f32_16x16x32_bf16 v[40:43], v[104:107], v[184:187], v[40:43]
	v_mfma_f32_16x16x32_bf16 v[28:31], v[88:91], v[192:195], v[28:31]
	v_mfma_f32_16x16x32_bf16 v[24:27], v[104:107], v[192:195], v[24:27]
	v_mfma_f32_16x16x32_bf16 v[12:15], v[88:91], v[200:203], v[12:15]
	v_mfma_f32_16x16x32_bf16 v[8:11], v[104:107], v[200:203], v[8:11]
	v_mfma_f32_16x16x32_bf16 v[60:63], v[92:95], v[180:183], v[60:63]
	v_mfma_f32_16x16x32_bf16 v[56:59], v[108:111], v[180:183], v[56:59]
	v_mfma_f32_16x16x32_bf16 v[44:47], v[92:95], v[188:191], v[44:47]
	v_mfma_f32_16x16x32_bf16 v[40:43], v[108:111], v[188:191], v[40:43]
	v_mfma_f32_16x16x32_bf16 v[28:31], v[92:95], v[196:199], v[28:31]
	v_mfma_f32_16x16x32_bf16 v[24:27], v[108:111], v[196:199], v[24:27]
	v_mfma_f32_16x16x32_bf16 v[12:15], v[92:95], v[204:207], v[12:15]
	v_mfma_f32_16x16x32_bf16 v[8:11], v[108:111], v[204:207], v[8:11]
	s_setprio 0
	s_barrier
	s_add_u32 s44, s42, 0x40000
	s_addc_u32 s45, s43, 0
	s_mov_b32 m0, s55
	s_nop 0
	global_load_lds_dwordx4 v146, s[44:45]
	s_mov_b32 m0, s56
	s_nop 0
	global_load_lds_dwordx4 v150, s[44:45]
	s_waitcnt vmcnt(6)
	s_barrier
	s_setprio 1
	v_mfma_f32_16x16x32_bf16 v[52:55], v[210:213], v[158:161], v[52:55]
	v_mfma_f32_16x16x32_bf16 v[48:51], v[218:221], v[158:161], v[48:51]
	v_mfma_f32_16x16x32_bf16 v[36:39], v[210:213], v[184:187], v[36:39]
	v_mfma_f32_16x16x32_bf16 v[32:35], v[218:221], v[184:187], v[32:35]
	v_mfma_f32_16x16x32_bf16 v[20:23], v[210:213], v[192:195], v[20:23]
	v_mfma_f32_16x16x32_bf16 v[16:19], v[218:221], v[192:195], v[16:19]
	v_mfma_f32_16x16x32_bf16 v[4:7], v[210:213], v[200:203], v[4:7]
	v_mfma_f32_16x16x32_bf16 v[0:3], v[218:221], v[200:203], v[0:3]
	v_mfma_f32_16x16x32_bf16 v[52:55], v[214:217], v[180:183], v[52:55]
	v_mfma_f32_16x16x32_bf16 v[48:51], v[222:225], v[180:183], v[48:51]
	v_mfma_f32_16x16x32_bf16 v[36:39], v[214:217], v[188:191], v[36:39]
	v_mfma_f32_16x16x32_bf16 v[32:35], v[222:225], v[188:191], v[32:35]
	v_mfma_f32_16x16x32_bf16 v[20:23], v[214:217], v[196:199], v[20:23]
	v_mfma_f32_16x16x32_bf16 v[16:19], v[222:225], v[196:199], v[16:19]
	v_mfma_f32_16x16x32_bf16 v[4:7], v[214:217], v[204:207], v[4:7]
	v_mfma_f32_16x16x32_bf16 v[0:3], v[222:225], v[204:207], v[0:3]
	s_setprio 0
	s_barrier
	ds_read_b128 v[88:91], v167
	ds_read_b128 v[92:95], v168
	ds_read_b128 v[104:107], v175
	ds_read_b128 v[108:111], v176
	s_add_u32 s44, s38, 0x40000
	s_addc_u32 s45, s39, 0
	s_mov_b32 m0, s57
	ds_read_b128 v[158:161], v179 offset:32768
	ds_read_b128 v[180:183], v179 offset:33792
	ds_read_b128 v[184:187], v179 offset:34816
	ds_read_b128 v[188:191], v179 offset:35840
	ds_read_b128 v[192:195], v179 offset:36864
	ds_read_b128 v[196:199], v179 offset:37888
	ds_read_b128 v[200:203], v179 offset:38912
	ds_read_b128 v[204:207], v179 offset:39936
	s_nop 0
	global_load_lds_dwordx4 v144, s[44:45]
	s_mov_b32 m0, s58
	s_nop 0
	global_load_lds_dwordx4 v148, s[44:45]
	s_waitcnt lgkmcnt(8)
	s_barrier
	s_waitcnt lgkmcnt(0)
	s_setprio 1
	s_waitcnt lgkmcnt(0)
	v_mfma_f32_16x16x32_bf16 v[140:143], v[88:91], v[158:161], v[140:143]
	v_mfma_f32_16x16x32_bf16 v[136:139], v[104:107], v[158:161], v[136:139]
	v_mfma_f32_16x16x32_bf16 v[124:127], v[88:91], v[184:187], v[124:127]
	v_mfma_f32_16x16x32_bf16 v[120:123], v[104:107], v[184:187], v[120:123]
	v_mfma_f32_16x16x32_bf16 v[100:103], v[88:91], v[192:195], v[100:103]
	v_mfma_f32_16x16x32_bf16 v[96:99], v[104:107], v[192:195], v[96:99]
	v_mfma_f32_16x16x32_bf16 v[76:79], v[88:91], v[200:203], v[76:79]
	v_mfma_f32_16x16x32_bf16 v[72:75], v[104:107], v[200:203], v[72:75]
	v_mfma_f32_16x16x32_bf16 v[140:143], v[92:95], v[180:183], v[140:143]
	v_mfma_f32_16x16x32_bf16 v[136:139], v[108:111], v[180:183], v[136:139]
	v_mfma_f32_16x16x32_bf16 v[124:127], v[92:95], v[188:191], v[124:127]
	v_mfma_f32_16x16x32_bf16 v[120:123], v[108:111], v[188:191], v[120:123]
	v_mfma_f32_16x16x32_bf16 v[100:103], v[92:95], v[196:199], v[100:103]
	v_mfma_f32_16x16x32_bf16 v[96:99], v[108:111], v[196:199], v[96:99]
	v_mfma_f32_16x16x32_bf16 v[76:79], v[92:95], v[204:207], v[76:79]
	v_mfma_f32_16x16x32_bf16 v[72:75], v[108:111], v[204:207], v[72:75]
	s_setprio 0
	s_barrier
	s_add_u32 s44, s42, 0x80
	s_addc_u32 s45, s43, 0
	s_mov_b32 m0, s61
	ds_read_b128 v[210:213], v169
	ds_read_b128 v[214:217], v170
	ds_read_b128 v[218:221], v177
	ds_read_b128 v[222:225], v178
	s_nop 0
	global_load_lds_dwordx4 v146, s[44:45]
	s_mov_b32 m0, s62
	s_nop 0
	global_load_lds_dwordx4 v150, s[44:45]
	s_nop 0
	s_barrier
	s_waitcnt lgkmcnt(0)
	s_setprio 1
	s_waitcnt lgkmcnt(0)
	v_mfma_f32_16x16x32_bf16 v[132:135], v[210:213], v[158:161], v[132:135]
	v_mfma_f32_16x16x32_bf16 v[128:131], v[218:221], v[158:161], v[128:131]
	v_mfma_f32_16x16x32_bf16 v[116:119], v[210:213], v[184:187], v[116:119]
	v_mfma_f32_16x16x32_bf16 v[112:115], v[218:221], v[184:187], v[112:115]
	v_mfma_f32_16x16x32_bf16 v[84:87], v[210:213], v[192:195], v[84:87]
	v_mfma_f32_16x16x32_bf16 v[80:83], v[218:221], v[192:195], v[80:83]
	v_mfma_f32_16x16x32_bf16 v[68:71], v[210:213], v[200:203], v[68:71]
	v_mfma_f32_16x16x32_bf16 v[64:67], v[218:221], v[200:203], v[64:67]
	v_mfma_f32_16x16x32_bf16 v[132:135], v[214:217], v[180:183], v[132:135]
	v_mfma_f32_16x16x32_bf16 v[128:131], v[222:225], v[180:183], v[128:131]
	v_mfma_f32_16x16x32_bf16 v[116:119], v[214:217], v[188:191], v[116:119]
	v_mfma_f32_16x16x32_bf16 v[112:115], v[222:225], v[188:191], v[112:115]
	v_mfma_f32_16x16x32_bf16 v[84:87], v[214:217], v[196:199], v[84:87]
	v_mfma_f32_16x16x32_bf16 v[80:83], v[222:225], v[196:199], v[80:83]
	v_mfma_f32_16x16x32_bf16 v[68:71], v[214:217], v[204:207], v[68:71]
	v_mfma_f32_16x16x32_bf16 v[64:67], v[222:225], v[204:207], v[64:67]
	s_setprio 0
	s_add_u32 s38, s38, 0x80
	s_addc_u32 s39, s39, 0
	s_mov_b32 m0, s63
	s_barrier
	ds_read_b128 v[158:161], v179 offset:49152
	ds_read_b128 v[180:183], v179 offset:50176
	ds_read_b128 v[184:187], v179 offset:51200
	ds_read_b128 v[188:191], v179 offset:52224
	ds_read_b128 v[192:195], v179 offset:53248
	ds_read_b128 v[196:199], v179 offset:54272
	ds_read_b128 v[200:203], v179 offset:55296
	ds_read_b128 v[204:207], v179 offset:56320
	s_nop 0
	global_load_lds_dwordx4 v144, s[38:39]
	s_mov_b32 m0, s64
	s_nop 0
	global_load_lds_dwordx4 v148, s[38:39]
	s_nop 0
	s_barrier
	s_waitcnt lgkmcnt(0)
	s_setprio 1
	s_waitcnt lgkmcnt(0)
	v_mfma_f32_16x16x32_bf16 v[60:63], v[88:91], v[158:161], v[60:63]
	v_mfma_f32_16x16x32_bf16 v[56:59], v[104:107], v[158:161], v[56:59]
	v_mfma_f32_16x16x32_bf16 v[44:47], v[88:91], v[184:187], v[44:47]
	v_mfma_f32_16x16x32_bf16 v[40:43], v[104:107], v[184:187], v[40:43]
	v_mfma_f32_16x16x32_bf16 v[28:31], v[88:91], v[192:195], v[28:31]
	v_mfma_f32_16x16x32_bf16 v[24:27], v[104:107], v[192:195], v[24:27]
	v_mfma_f32_16x16x32_bf16 v[12:15], v[88:91], v[200:203], v[12:15]
	v_mfma_f32_16x16x32_bf16 v[8:11], v[104:107], v[200:203], v[8:11]
	v_mfma_f32_16x16x32_bf16 v[60:63], v[92:95], v[180:183], v[60:63]
	v_mfma_f32_16x16x32_bf16 v[56:59], v[108:111], v[180:183], v[56:59]
	v_mfma_f32_16x16x32_bf16 v[44:47], v[92:95], v[188:191], v[44:47]
	v_mfma_f32_16x16x32_bf16 v[40:43], v[108:111], v[188:191], v[40:43]
	v_mfma_f32_16x16x32_bf16 v[28:31], v[92:95], v[196:199], v[28:31]
	v_mfma_f32_16x16x32_bf16 v[24:27], v[108:111], v[196:199], v[24:27]
	v_mfma_f32_16x16x32_bf16 v[12:15], v[92:95], v[204:207], v[12:15]
	v_mfma_f32_16x16x32_bf16 v[8:11], v[108:111], v[204:207], v[8:11]
	s_setprio 0
	s_barrier
	s_add_u32 s38, s42, 0x40080
	s_addc_u32 s39, s43, 0
	s_mov_b32 m0, s65
	s_nop 0
	global_load_lds_dwordx4 v146, s[38:39]
	s_mov_b32 m0, s66
	s_nop 0
	global_load_lds_dwordx4 v150, s[38:39]
	s_waitcnt vmcnt(6)
	s_barrier
	s_setprio 1
	v_mfma_f32_16x16x32_bf16 v[52:55], v[210:213], v[158:161], v[52:55]
	v_mfma_f32_16x16x32_bf16 v[48:51], v[218:221], v[158:161], v[48:51]
	v_mfma_f32_16x16x32_bf16 v[36:39], v[210:213], v[184:187], v[36:39]
	v_mfma_f32_16x16x32_bf16 v[32:35], v[218:221], v[184:187], v[32:35]
	v_mfma_f32_16x16x32_bf16 v[20:23], v[210:213], v[192:195], v[20:23]
	v_mfma_f32_16x16x32_bf16 v[16:19], v[218:221], v[192:195], v[16:19]
	v_mfma_f32_16x16x32_bf16 v[4:7], v[210:213], v[200:203], v[4:7]
	v_mfma_f32_16x16x32_bf16 v[0:3], v[218:221], v[200:203], v[0:3]
	v_mfma_f32_16x16x32_bf16 v[52:55], v[214:217], v[180:183], v[52:55]
	v_mfma_f32_16x16x32_bf16 v[48:51], v[222:225], v[180:183], v[48:51]
	v_mfma_f32_16x16x32_bf16 v[36:39], v[214:217], v[188:191], v[36:39]
	v_mfma_f32_16x16x32_bf16 v[32:35], v[222:225], v[188:191], v[32:35]
	v_mfma_f32_16x16x32_bf16 v[20:23], v[214:217], v[196:199], v[20:23]
	v_mfma_f32_16x16x32_bf16 v[16:19], v[222:225], v[196:199], v[16:19]
	v_mfma_f32_16x16x32_bf16 v[4:7], v[214:217], v[204:207], v[4:7]
	v_mfma_f32_16x16x32_bf16 v[0:3], v[222:225], v[204:207], v[0:3]
	s_setprio 0
	s_add_i32 s20, s20, 2
	s_cmp_gt_u32 s20, 13
	s_mov_b64 s[38:39], s[40:41]
	s_barrier
	s_cbranch_scc0 .LBB0_558
	s_cmpk_gt_i32 s2, 0x7f
	s_cselect_b64 s[34:35], -1, 0
	v_mov_b32_e32 v88, v162
	s_mov_b64 s[8:9], 0xc000
	s_and_b64 vcc, exec, s[34:35]
	s_cbranch_vccnz .LBB0_561
	s_ashr_i32 s1, s2, 31
	s_lshr_b32 s1, s1, 28
	s_add_i32 s1, s2, s1
	s_ashr_i32 s1, s1, 4
	s_mul_hi_i32 s9, s1, 0x1800
	s_mul_i32 s8, s1, 0x1800

.LBB0_1557:
	s_ashr_i32 s25, s24, 31
	s_lshl_b64 s[26:27], s[24:25], 19
	s_add_u32 s26, s45, s26
	s_addc_u32 s27, s46, s27
	s_ashr_i32 s23, s22, 31
	s_lshl_b64 s[28:29], s[22:23], 19
	s_add_u32 s28, s43, s28
	s_addc_u32 s29, s44, s29
	s_and_b64 s[34:35], s[14:15], exec
	v_mov_b32_e32 v0, 0
	s_cselect_b32 s1, s29, s5
	s_cselect_b32 s10, s28, s4
	s_mov_b32 s23, -2
	s_mov_b64 s[34:35], 0
	s_waitcnt lgkmcnt(0)
	v_mov_b32_e32 v1, 0
	v_mov_b64_e32 v[2:3], 0
	v_mov_b64_e32 v[4:5], 0
	v_mov_b64_e32 v[6:7], 0
	v_mov_b64_e32 v[8:9], 0
	v_mov_b64_e32 v[10:11], 0
	v_mov_b64_e32 v[12:13], 0
	v_mov_b64_e32 v[14:15], 0
	v_mov_b64_e32 v[16:17], 0
	v_mov_b64_e32 v[18:19], 0
	v_mov_b64_e32 v[20:21], 0
	v_mov_b64_e32 v[22:23], 0
	v_mov_b64_e32 v[24:25], 0
	v_mov_b64_e32 v[26:27], 0
	v_mov_b64_e32 v[28:29], 0
	v_mov_b64_e32 v[30:31], 0
	v_mov_b64_e32 v[40:41], 0
	v_mov_b64_e32 v[42:43], 0
	v_mov_b64_e32 v[44:45], 0
	v_mov_b64_e32 v[46:47], 0
	v_mov_b64_e32 v[56:57], 0
	v_mov_b64_e32 v[58:59], 0
	v_mov_b64_e32 v[60:61], 0
	v_mov_b64_e32 v[62:63], 0
	v_mov_b64_e32 v[64:65], 0
	v_mov_b64_e32 v[66:67], 0
	v_mov_b64_e32 v[68:69], 0
	v_mov_b64_e32 v[70:71], 0
	v_mov_b64_e32 v[72:73], 0
	v_mov_b64_e32 v[74:75], 0
	v_mov_b64_e32 v[76:77], 0
	v_mov_b64_e32 v[78:79], 0
	v_mov_b64_e32 v[80:81], 0
	v_mov_b64_e32 v[82:83], 0
	v_mov_b64_e32 v[84:85], 0
	v_mov_b64_e32 v[86:87], 0
	v_mov_b64_e32 v[96:97], 0
	v_mov_b64_e32 v[98:99], 0
	v_mov_b64_e32 v[100:101], 0
	v_mov_b64_e32 v[102:103], 0
	v_mov_b64_e32 v[112:113], 0
	v_mov_b64_e32 v[114:115], 0
	v_mov_b32_e32 v116, 0
	v_mov_b64_e32 v[88:89], 0
	v_mov_b64_e32 v[90:91], 0
	v_mov_b64_e32 v[92:93], 0
	v_mov_b64_e32 v[94:95], 0
	v_mov_b64_e32 v[104:105], 0
	v_mov_b64_e32 v[106:107], 0
	v_mov_b64_e32 v[108:109], 0
	v_mov_b64_e32 v[110:111], 0
	v_mov_b32_e32 v117, 0
	v_mov_b64_e32 v[118:119], 0
	v_mov_b64_e32 v[120:121], 0
	v_mov_b64_e32 v[122:123], 0
	v_mov_b64_e32 v[124:125], 0
	v_mov_b64_e32 v[126:127], 0
	v_mov_b64_e32 v[128:129], 0
	v_mov_b64_e32 v[130:131], 0
	v_mov_b64_e32 v[132:133], 0
	v_mov_b64_e32 v[134:135], 0
	v_mov_b64_e32 v[136:137], 0
	v_mov_b64_e32 v[138:139], 0
	v_mov_b64_e32 v[140:141], 0
	v_mov_b64_e32 v[142:143], 0

.LBB0_2525:
	s_ashr_i32 s27, s26, 31
	s_lshl_b64 s[28:29], s[26:27], 19
	s_add_u32 s28, s43, s28
	s_addc_u32 s29, s44, s29
	s_ashr_i32 s25, s24, 31
	s_lshl_b64 s[30:31], s[24:25], 19
	s_add_u32 s30, s45, s30
	s_addc_u32 s31, s46, s31
	s_and_b64 s[34:35], s[14:15], exec
	v_mov_b32_e32 v0, 0
	s_cselect_b32 s1, s31, s3
	s_cselect_b32 s20, s30, s2
	s_mov_b32 s25, -2
	s_mov_b64 s[34:35], 0
	s_waitcnt lgkmcnt(0)
	v_mov_b32_e32 v1, v0
	v_mov_b32_e32 v2, v0
	v_mov_b32_e32 v3, v0
	v_mov_b32_e32 v4, v0
	v_mov_b32_e32 v5, v0
	v_mov_b32_e32 v6, v0
	v_mov_b32_e32 v7, v0
	v_mov_b32_e32 v16, v0
	v_mov_b32_e32 v17, v0
	v_mov_b32_e32 v18, v0
	v_mov_b32_e32 v19, v0
	v_mov_b32_e32 v20, v0
	v_mov_b32_e32 v21, v0
	v_mov_b32_e32 v22, v0
	v_mov_b32_e32 v23, v0
	v_mov_b32_e32 v32, v0
	v_mov_b32_e32 v33, v0
	v_mov_b32_e32 v34, v0
	v_mov_b32_e32 v35, v0
	v_mov_b32_e32 v36, v0
	v_mov_b32_e32 v37, v0
	v_mov_b32_e32 v38, v0
	v_mov_b32_e32 v39, v0
	v_mov_b32_e32 v48, v0
	v_mov_b32_e32 v49, v0
	v_mov_b32_e32 v50, v0
	v_mov_b32_e32 v51, v0
	v_mov_b64_e32 v[8:9], 0
	v_mov_b64_e32 v[10:11], 0
	v_mov_b64_e32 v[12:13], 0
	v_mov_b64_e32 v[14:15], 0
	v_mov_b64_e32 v[24:25], 0
	v_mov_b64_e32 v[26:27], 0
	v_mov_b64_e32 v[28:29], 0
	v_mov_b64_e32 v[30:31], 0
	v_mov_b64_e32 v[40:41], 0
	v_mov_b64_e32 v[42:43], 0
	v_mov_b64_e32 v[44:45], 0
	v_mov_b64_e32 v[46:47], 0
	v_mov_b64_e32 v[52:53], 0
	v_mov_b64_e32 v[54:55], 0
	v_mov_b64_e32 v[56:57], 0
	v_mov_b64_e32 v[58:59], 0
	v_mov_b64_e32 v[60:61], 0
	v_mov_b64_e32 v[62:63], 0
	v_mov_b64_e32 v[64:65], 0
	v_mov_b64_e32 v[66:67], 0
	v_mov_b64_e32 v[68:69], 0
	v_mov_b64_e32 v[70:71], 0
	v_mov_b64_e32 v[72:73], 0
	v_mov_b64_e32 v[74:75], 0
	v_mov_b64_e32 v[76:77], 0
	v_mov_b64_e32 v[78:79], 0
	v_mov_b64_e32 v[80:81], 0
	v_mov_b64_e32 v[82:83], 0
	v_mov_b64_e32 v[84:85], 0
	v_mov_b64_e32 v[86:87], 0
	v_mov_b64_e32 v[88:89], 0
	v_mov_b64_e32 v[90:91], 0
	v_mov_b64_e32 v[96:97], 0
	v_mov_b64_e32 v[98:99], 0
	v_mov_b64_e32 v[112:113], 0
	v_mov_b64_e32 v[114:115], 0
	v_mov_b64_e32 v[116:117], 0
	v_mov_b64_e32 v[118:119], 0
	v_mov_b64_e32 v[120:121], 0
	v_mov_b64_e32 v[122:123], 0
	v_mov_b64_e32 v[124:125], 0
	v_mov_b64_e32 v[126:127], 0
	v_mov_b64_e32 v[128:129], 0
	v_mov_b64_e32 v[130:131], 0
	v_mov_b64_e32 v[132:133], 0
	v_mov_b64_e32 v[134:135], 0
	v_mov_b64_e32 v[136:137], 0
	v_mov_b64_e32 v[138:139], 0
	v_mov_b64_e32 v[140:141], 0
	v_mov_b64_e32 v[142:143], 0
.LBB0_2526:
	s_add_u32 s36, s34, 0x100
	ds_read_b128 v[92:95], v165
	ds_read_b128 v[100:103], v166
	ds_read_b128 v[104:107], v173
	ds_read_b128 v[108:111], v174
	s_addc_u32 s37, s35, 0
	s_and_b32 s27, s36, 0x700
	s_add_u32 s33, s2, s27
	s_addc_u32 s65, s3, 0
	s_cmp_eq_u32 s25, 12
	s_cselect_b64 s[40:41], -1, 0
	s_and_b64 s[38:39], s[40:41], exec
	s_cselect_b32 s39, s1, s65
	s_cselect_b32 s38, s20, s33
	s_cselect_b32 s33, 0, 0
	s_cselect_b32 s27, 0, s27
	s_add_u32 s34, s4, s34
	s_addc_u32 s35, s5, s35
	s_add_u32 s34, s34, 0x40080
	s_addc_u32 s35, s35, 0
	ds_read_b128 v[158:161], v181
	ds_read_b128 v[182:185], v181 offset:1024
	ds_read_b128 v[186:189], v181 offset:2048
	ds_read_b128 v[190:193], v181 offset:3072
	ds_read_b128 v[194:197], v181 offset:4096
	ds_read_b128 v[198:201], v181 offset:5120
	ds_read_b128 v[202:205], v181 offset:6144
	ds_read_b128 v[210:213], v181 offset:7168
	s_add_i32 m0, s13, 0xc000
	s_nop 0
	global_load_lds_dwordx4 v144, s[34:35]
	s_add_i32 m0, s13, 0xe000
	s_nop 0
	global_load_lds_dwordx4 v148, s[34:35]
	s_waitcnt lgkmcnt(8)
	s_nop 0
	s_barrier
	s_waitcnt lgkmcnt(0)
	s_setprio 1
	s_waitcnt lgkmcnt(0)
	v_mfma_f32_16x16x32_bf16 v[140:143], v[92:95], v[158:161], v[140:143]
	v_mfma_f32_16x16x32_bf16 v[136:139], v[104:107], v[158:161], v[136:139]
	v_mfma_f32_16x16x32_bf16 v[124:127], v[92:95], v[186:189], v[124:127]
	v_mfma_f32_16x16x32_bf16 v[120:123], v[104:107], v[186:189], v[120:123]
	v_mfma_f32_16x16x32_bf16 v[96:99], v[92:95], v[194:197], v[96:99]
	v_mfma_f32_16x16x32_bf16 v[88:91], v[104:107], v[194:197], v[88:91]
	v_mfma_f32_16x16x32_bf16 v[76:79], v[92:95], v[202:205], v[76:79]
	v_mfma_f32_16x16x32_bf16 v[72:75], v[104:107], v[202:205], v[72:75]
	v_mfma_f32_16x16x32_bf16 v[140:143], v[100:103], v[182:185], v[140:143]
	v_mfma_f32_16x16x32_bf16 v[136:139], v[108:111], v[182:185], v[136:139]
	v_mfma_f32_16x16x32_bf16 v[124:127], v[100:103], v[190:193], v[124:127]
	v_mfma_f32_16x16x32_bf16 v[120:123], v[108:111], v[190:193], v[120:123]
	v_mfma_f32_16x16x32_bf16 v[96:99], v[100:103], v[198:201], v[96:99]
	v_mfma_f32_16x16x32_bf16 v[88:91], v[108:111], v[198:201], v[88:91]
	v_mfma_f32_16x16x32_bf16 v[76:79], v[100:103], v[210:213], v[76:79]
	v_mfma_f32_16x16x32_bf16 v[72:75], v[108:111], v[210:213], v[72:75]
	s_setprio 0
	s_barrier
	s_mov_b64 s[34:35], s[38:39]
	s_mov_b32 m0, s47
	ds_read_b128 v[214:217], v167
	ds_read_b128 v[218:221], v168
	ds_read_b128 v[222:225], v175
	ds_read_b128 v[226:229], v176
	s_nop 0
	global_load_lds_dwordx4 v146, s[34:35]
	s_mov_b32 m0, s48
	s_nop 0
	global_load_lds_dwordx4 v150, s[34:35]
	s_nop 0
	s_barrier
	s_waitcnt lgkmcnt(0)
	s_setprio 1
	s_waitcnt lgkmcnt(0)
	v_mfma_f32_16x16x32_bf16 v[132:135], v[214:217], v[158:161], v[132:135]
	v_mfma_f32_16x16x32_bf16 v[128:131], v[222:225], v[158:161], v[128:131]
	v_mfma_f32_16x16x32_bf16 v[116:119], v[214:217], v[186:189], v[116:119]
	v_mfma_f32_16x16x32_bf16 v[112:115], v[222:225], v[186:189], v[112:115]
	v_mfma_f32_16x16x32_bf16 v[84:87], v[214:217], v[194:197], v[84:87]
	v_mfma_f32_16x16x32_bf16 v[80:83], v[222:225], v[194:197], v[80:83]
	v_mfma_f32_16x16x32_bf16 v[68:71], v[214:217], v[202:205], v[68:71]
	v_mfma_f32_16x16x32_bf16 v[64:67], v[222:225], v[202:205], v[64:67]
	v_mfma_f32_16x16x32_bf16 v[132:135], v[218:221], v[182:185], v[132:135]
	v_mfma_f32_16x16x32_bf16 v[128:131], v[226:229], v[182:185], v[128:131]
	v_mfma_f32_16x16x32_bf16 v[116:119], v[218:221], v[190:193], v[116:119]
	v_mfma_f32_16x16x32_bf16 v[112:115], v[226:229], v[190:193], v[112:115]
	v_mfma_f32_16x16x32_bf16 v[84:87], v[218:221], v[198:201], v[84:87]
	v_mfma_f32_16x16x32_bf16 v[80:83], v[226:229], v[198:201], v[80:83]
	v_mfma_f32_16x16x32_bf16 v[68:71], v[218:221], v[210:213], v[68:71]
	v_mfma_f32_16x16x32_bf16 v[64:67], v[226:229], v[210:213], v[64:67]
	s_setprio 0
	s_and_b64 s[34:35], s[14:15], s[40:41]
	s_and_b64 s[34:35], s[34:35], exec
	s_cselect_b32 s34, s28, s4
	s_cselect_b32 s35, s29, s5
	s_add_u32 s34, s34, s27
	s_addc_u32 s35, s35, s33
	s_mov_b64 s[40:41], s[34:35]
	s_mov_b32 m0, s13
	s_barrier
	ds_read_b128 v[158:161], v181 offset:16384
	ds_read_b128 v[182:185], v181 offset:17408
	ds_read_b128 v[186:189], v181 offset:18432
	ds_read_b128 v[190:193], v181 offset:19456
	ds_read_b128 v[194:197], v181 offset:20480
	ds_read_b128 v[198:201], v181 offset:21504
	ds_read_b128 v[202:205], v181 offset:22528
	ds_read_b128 v[210:213], v181 offset:23552
	s_nop 0
	global_load_lds_dwordx4 v144, s[40:41]
	s_mov_b32 m0, s49
	s_nop 0
	global_load_lds_dwordx4 v148, s[40:41]
	s_nop 0
	s_barrier
	s_waitcnt lgkmcnt(0)
	s_setprio 1
	s_waitcnt lgkmcnt(0)
	v_mfma_f32_16x16x32_bf16 v[60:63], v[92:95], v[158:161], v[60:63]
	v_mfma_f32_16x16x32_bf16 v[56:59], v[104:107], v[158:161], v[56:59]
	v_mfma_f32_16x16x32_bf16 v[44:47], v[92:95], v[186:189], v[44:47]
	v_mfma_f32_16x16x32_bf16 v[40:43], v[104:107], v[186:189], v[40:43]
	v_mfma_f32_16x16x32_bf16 v[28:31], v[92:95], v[194:197], v[28:31]
	v_mfma_f32_16x16x32_bf16 v[24:27], v[104:107], v[194:197], v[24:27]
	v_mfma_f32_16x16x32_bf16 v[12:15], v[92:95], v[202:205], v[12:15]
	v_mfma_f32_16x16x32_bf16 v[8:11], v[104:107], v[202:205], v[8:11]
	v_mfma_f32_16x16x32_bf16 v[60:63], v[100:103], v[182:185], v[60:63]
	v_mfma_f32_16x16x32_bf16 v[56:59], v[108:111], v[182:185], v[56:59]
	v_mfma_f32_16x16x32_bf16 v[44:47], v[100:103], v[190:193], v[44:47]
	v_mfma_f32_16x16x32_bf16 v[40:43], v[108:111], v[190:193], v[40:43]
	v_mfma_f32_16x16x32_bf16 v[28:31], v[100:103], v[198:201], v[28:31]
	v_mfma_f32_16x16x32_bf16 v[24:27], v[108:111], v[198:201], v[24:27]
	v_mfma_f32_16x16x32_bf16 v[12:15], v[100:103], v[210:213], v[12:15]
	v_mfma_f32_16x16x32_bf16 v[8:11], v[108:111], v[210:213], v[8:11]
	s_setprio 0
	s_barrier
	s_add_u32 s40, s38, 0x40000
	s_addc_u32 s41, s39, 0
	s_mov_b32 m0, s50
	s_nop 0
	global_load_lds_dwordx4 v146, s[40:41]
	s_mov_b32 m0, s51
	s_nop 0
	global_load_lds_dwordx4 v150, s[40:41]
	s_waitcnt vmcnt(6)
	s_barrier
	s_setprio 1
	v_mfma_f32_16x16x32_bf16 v[52:55], v[214:217], v[158:161], v[52:55]
	v_mfma_f32_16x16x32_bf16 v[48:51], v[222:225], v[158:161], v[48:51]
	v_mfma_f32_16x16x32_bf16 v[36:39], v[214:217], v[186:189], v[36:39]
	v_mfma_f32_16x16x32_bf16 v[32:35], v[222:225], v[186:189], v[32:35]
	v_mfma_f32_16x16x32_bf16 v[20:23], v[214:217], v[194:197], v[20:23]
	v_mfma_f32_16x16x32_bf16 v[16:19], v[222:225], v[194:197], v[16:19]
	v_mfma_f32_16x16x32_bf16 v[4:7], v[214:217], v[202:205], v[4:7]
	v_mfma_f32_16x16x32_bf16 v[0:3], v[222:225], v[202:205], v[0:3]
	v_mfma_f32_16x16x32_bf16 v[52:55], v[218:221], v[182:185], v[52:55]
	v_mfma_f32_16x16x32_bf16 v[48:51], v[226:229], v[182:185], v[48:51]
	v_mfma_f32_16x16x32_bf16 v[36:39], v[218:221], v[190:193], v[36:39]
	v_mfma_f32_16x16x32_bf16 v[32:35], v[226:229], v[190:193], v[32:35]
	v_mfma_f32_16x16x32_bf16 v[20:23], v[218:221], v[198:201], v[20:23]
	v_mfma_f32_16x16x32_bf16 v[16:19], v[226:229], v[198:201], v[16:19]
	v_mfma_f32_16x16x32_bf16 v[4:7], v[218:221], v[210:213], v[4:7]
	v_mfma_f32_16x16x32_bf16 v[0:3], v[226:229], v[210:213], v[0:3]
	s_setprio 0
	s_barrier
	ds_read_b128 v[92:95], v169
	ds_read_b128 v[100:103], v170
	ds_read_b128 v[104:107], v177
	ds_read_b128 v[108:111], v178
	s_add_u32 s40, s34, 0x40000
	s_addc_u32 s41, s35, 0
	s_mov_b32 m0, s52
	ds_read_b128 v[158:161], v181 offset:32768
	ds_read_b128 v[182:185], v181 offset:33792
	ds_read_b128 v[186:189], v181 offset:34816
	ds_read_b128 v[190:193], v181 offset:35840
	ds_read_b128 v[194:197], v181 offset:36864
	ds_read_b128 v[198:201], v181 offset:37888
	ds_read_b128 v[202:205], v181 offset:38912
	ds_read_b128 v[210:213], v181 offset:39936
	s_nop 0
	global_load_lds_dwordx4 v144, s[40:41]
	s_mov_b32 m0, s53
	s_nop 0
	global_load_lds_dwordx4 v148, s[40:41]
	s_waitcnt lgkmcnt(8)
	s_barrier
	s_waitcnt lgkmcnt(0)
	s_setprio 1
	s_waitcnt lgkmcnt(0)
	v_mfma_f32_16x16x32_bf16 v[140:143], v[92:95], v[158:161], v[140:143]
	v_mfma_f32_16x16x32_bf16 v[136:139], v[104:107], v[158:161], v[136:139]
	v_mfma_f32_16x16x32_bf16 v[124:127], v[92:95], v[186:189], v[124:127]
	v_mfma_f32_16x16x32_bf16 v[120:123], v[104:107], v[186:189], v[120:123]
	v_mfma_f32_16x16x32_bf16 v[96:99], v[92:95], v[194:197], v[96:99]
	v_mfma_f32_16x16x32_bf16 v[88:91], v[104:107], v[194:197], v[88:91]
	v_mfma_f32_16x16x32_bf16 v[76:79], v[92:95], v[202:205], v[76:79]
	v_mfma_f32_16x16x32_bf16 v[72:75], v[104:107], v[202:205], v[72:75]
	v_mfma_f32_16x16x32_bf16 v[140:143], v[100:103], v[182:185], v[140:143]
	v_mfma_f32_16x16x32_bf16 v[136:139], v[108:111], v[182:185], v[136:139]
	v_mfma_f32_16x16x32_bf16 v[124:127], v[100:103], v[190:193], v[124:127]
	v_mfma_f32_16x16x32_bf16 v[120:123], v[108:111], v[190:193], v[120:123]
	v_mfma_f32_16x16x32_bf16 v[96:99], v[100:103], v[198:201], v[96:99]
	v_mfma_f32_16x16x32_bf16 v[88:91], v[108:111], v[198:201], v[88:91]
	v_mfma_f32_16x16x32_bf16 v[76:79], v[100:103], v[210:213], v[76:79]
	v_mfma_f32_16x16x32_bf16 v[72:75], v[108:111], v[210:213], v[72:75]
	s_setprio 0
	s_barrier
	s_add_u32 s40, s38, 0x80
	s_addc_u32 s41, s39, 0
	s_mov_b32 m0, s56
	ds_read_b128 v[214:217], v171
	ds_read_b128 v[218:221], v172
	ds_read_b128 v[222:225], v179
	ds_read_b128 v[226:229], v180
	s_nop 0
	global_load_lds_dwordx4 v146, s[40:41]
	s_mov_b32 m0, s57
	s_nop 0
	global_load_lds_dwordx4 v150, s[40:41]
	s_nop 0
	s_barrier
	s_waitcnt lgkmcnt(0)
	s_setprio 1
	s_waitcnt lgkmcnt(0)
	v_mfma_f32_16x16x32_bf16 v[132:135], v[214:217], v[158:161], v[132:135]
	v_mfma_f32_16x16x32_bf16 v[128:131], v[222:225], v[158:161], v[128:131]
	v_mfma_f32_16x16x32_bf16 v[116:119], v[214:217], v[186:189], v[116:119]
	v_mfma_f32_16x16x32_bf16 v[112:115], v[222:225], v[186:189], v[112:115]
	v_mfma_f32_16x16x32_bf16 v[84:87], v[214:217], v[194:197], v[84:87]
	v_mfma_f32_16x16x32_bf16 v[80:83], v[222:225], v[194:197], v[80:83]
	v_mfma_f32_16x16x32_bf16 v[68:71], v[214:217], v[202:205], v[68:71]
	v_mfma_f32_16x16x32_bf16 v[64:67], v[222:225], v[202:205], v[64:67]
	v_mfma_f32_16x16x32_bf16 v[132:135], v[218:221], v[182:185], v[132:135]
	v_mfma_f32_16x16x32_bf16 v[128:131], v[226:229], v[182:185], v[128:131]
	v_mfma_f32_16x16x32_bf16 v[116:119], v[218:221], v[190:193], v[116:119]
	v_mfma_f32_16x16x32_bf16 v[112:115], v[226:229], v[190:193], v[112:115]
	v_mfma_f32_16x16x32_bf16 v[84:87], v[218:221], v[198:201], v[84:87]
	v_mfma_f32_16x16x32_bf16 v[80:83], v[226:229], v[198:201], v[80:83]
	v_mfma_f32_16x16x32_bf16 v[68:71], v[218:221], v[210:213], v[68:71]
	v_mfma_f32_16x16x32_bf16 v[64:67], v[226:229], v[210:213], v[64:67]
	s_setprio 0
	s_add_u32 s34, s34, 0x80
	s_addc_u32 s35, s35, 0
	s_mov_b32 m0, s58
	s_barrier
	ds_read_b128 v[158:161], v181 offset:49152
	ds_read_b128 v[182:185], v181 offset:50176
	ds_read_b128 v[186:189], v181 offset:51200
	ds_read_b128 v[190:193], v181 offset:52224
	ds_read_b128 v[194:197], v181 offset:53248
	ds_read_b128 v[198:201], v181 offset:54272
	ds_read_b128 v[202:205], v181 offset:55296
	ds_read_b128 v[210:213], v181 offset:56320
	s_nop 0
	global_load_lds_dwordx4 v144, s[34:35]
	s_mov_b32 m0, s59
	s_nop 0
	global_load_lds_dwordx4 v148, s[34:35]
	s_nop 0
	s_barrier
	s_waitcnt lgkmcnt(0)
	s_setprio 1
	s_waitcnt lgkmcnt(0)
	v_mfma_f32_16x16x32_bf16 v[60:63], v[92:95], v[158:161], v[60:63]
	v_mfma_f32_16x16x32_bf16 v[56:59], v[104:107], v[158:161], v[56:59]
	v_mfma_f32_16x16x32_bf16 v[44:47], v[92:95], v[186:189], v[44:47]
	v_mfma_f32_16x16x32_bf16 v[40:43], v[104:107], v[186:189], v[40:43]
	v_mfma_f32_16x16x32_bf16 v[28:31], v[92:95], v[194:197], v[28:31]
	v_mfma_f32_16x16x32_bf16 v[24:27], v[104:107], v[194:197], v[24:27]
	v_mfma_f32_16x16x32_bf16 v[12:15], v[92:95], v[202:205], v[12:15]
	v_mfma_f32_16x16x32_bf16 v[8:11], v[104:107], v[202:205], v[8:11]
	v_mfma_f32_16x16x32_bf16 v[60:63], v[100:103], v[182:185], v[60:63]
	v_mfma_f32_16x16x32_bf16 v[56:59], v[108:111], v[182:185], v[56:59]
	v_mfma_f32_16x16x32_bf16 v[44:47], v[100:103], v[190:193], v[44:47]
	v_mfma_f32_16x16x32_bf16 v[40:43], v[108:111], v[190:193], v[40:43]
	v_mfma_f32_16x16x32_bf16 v[28:31], v[100:103], v[198:201], v[28:31]
	v_mfma_f32_16x16x32_bf16 v[24:27], v[108:111], v[198:201], v[24:27]
	v_mfma_f32_16x16x32_bf16 v[12:15], v[100:103], v[210:213], v[12:15]
	v_mfma_f32_16x16x32_bf16 v[8:11], v[108:111], v[210:213], v[8:11]
	s_setprio 0
	s_barrier
	s_add_u32 s34, s38, 0x40080
	s_addc_u32 s35, s39, 0
	s_mov_b32 m0, s60
	s_nop 0
	global_load_lds_dwordx4 v146, s[34:35]
	s_mov_b32 m0, s61
	s_nop 0
	global_load_lds_dwordx4 v150, s[34:35]
	s_waitcnt vmcnt(6)
	s_barrier
	s_setprio 1
	v_mfma_f32_16x16x32_bf16 v[52:55], v[214:217], v[158:161], v[52:55]
	v_mfma_f32_16x16x32_bf16 v[48:51], v[222:225], v[158:161], v[48:51]
	v_mfma_f32_16x16x32_bf16 v[36:39], v[214:217], v[186:189], v[36:39]
	v_mfma_f32_16x16x32_bf16 v[32:35], v[222:225], v[186:189], v[32:35]
	v_mfma_f32_16x16x32_bf16 v[20:23], v[214:217], v[194:197], v[20:23]
	v_mfma_f32_16x16x32_bf16 v[16:19], v[222:225], v[194:197], v[16:19]
	v_mfma_f32_16x16x32_bf16 v[4:7], v[214:217], v[202:205], v[4:7]
	v_mfma_f32_16x16x32_bf16 v[0:3], v[222:225], v[202:205], v[0:3]
	v_mfma_f32_16x16x32_bf16 v[52:55], v[218:221], v[182:185], v[52:55]
	v_mfma_f32_16x16x32_bf16 v[48:51], v[226:229], v[182:185], v[48:51]
	v_mfma_f32_16x16x32_bf16 v[36:39], v[218:221], v[190:193], v[36:39]
	v_mfma_f32_16x16x32_bf16 v[32:35], v[226:229], v[190:193], v[32:35]
	v_mfma_f32_16x16x32_bf16 v[20:23], v[218:221], v[198:201], v[20:23]
	v_mfma_f32_16x16x32_bf16 v[16:19], v[226:229], v[198:201], v[16:19]
	v_mfma_f32_16x16x32_bf16 v[4:7], v[218:221], v[210:213], v[4:7]
	v_mfma_f32_16x16x32_bf16 v[0:3], v[226:229], v[210:213], v[0:3]
	s_setprio 0
	s_add_i32 s25, s25, 2
	s_cmp_gt_u32 s25, 13
	s_mov_b64 s[34:35], s[36:37]
	s_barrier
	s_cbranch_scc0 .LBB0_2526
	v_mov_b32_e32 v92, v164
	s_cmpk_gt_i32 s0, 0x7f
	s_mov_b64 s[2:3], 0xc000
	s_cbranch_scc1 .LBB0_2529
	s_ashr_i32 s1, s0, 31
	s_lshr_b32 s1, s1, 28
	s_add_i32 s1, s0, s1
	s_ashr_i32 s1, s1, 4
	s_mul_hi_i32 s3, s1, 0x1800
	s_mul_i32 s2, s1, 0x1800

.LBB0_3520:
	s_ashr_i32 s35, s34, 31
	s_lshl_b64 s[36:37], s[34:35], 19
	s_add_u32 s36, s53, s36
	s_addc_u32 s37, s54, s37
	s_ashr_i32 s31, s30, 31
	s_lshl_b64 s[38:39], s[30:31], 19
	s_add_u32 s38, s55, s38
	s_addc_u32 s39, s56, s39
	s_and_b64 s[44:45], s[6:7], exec
	v_mov_b32_e32 v0, 0
	s_cselect_b32 s1, s39, s41
	s_cselect_b32 s3, s38, s40
	s_mov_b32 s16, -2
	s_mov_b64 s[44:45], 0
	s_waitcnt lgkmcnt(0)
	v_mov_b32_e32 v1, 0
	v_mov_b64_e32 v[2:3], 0
	v_mov_b64_e32 v[4:5], 0
	v_mov_b64_e32 v[6:7], 0
	v_mov_b64_e32 v[8:9], 0
	v_mov_b64_e32 v[10:11], 0
	v_mov_b64_e32 v[12:13], 0
	v_mov_b64_e32 v[14:15], 0
	v_mov_b64_e32 v[16:17], 0
	v_mov_b64_e32 v[18:19], 0
	v_mov_b64_e32 v[20:21], 0
	v_mov_b64_e32 v[22:23], 0
	v_mov_b64_e32 v[24:25], 0
	v_mov_b64_e32 v[26:27], 0
	v_mov_b64_e32 v[28:29], 0
	v_mov_b64_e32 v[30:31], 0
	v_mov_b64_e32 v[32:33], 0
	v_mov_b64_e32 v[34:35], 0
	v_mov_b64_e32 v[36:37], 0
	v_mov_b64_e32 v[38:39], 0
	v_mov_b64_e32 v[40:41], 0
	v_mov_b64_e32 v[42:43], 0
	v_mov_b64_e32 v[44:45], 0
	v_mov_b64_e32 v[46:47], 0
	v_mov_b64_e32 v[48:49], 0
	v_mov_b64_e32 v[50:51], 0
	v_mov_b64_e32 v[52:53], 0
	v_mov_b64_e32 v[54:55], 0
	v_mov_b64_e32 v[56:57], 0
	v_mov_b64_e32 v[58:59], 0
	v_mov_b64_e32 v[60:61], 0
	v_mov_b64_e32 v[62:63], 0
	v_mov_b64_e32 v[64:65], 0
	v_mov_b64_e32 v[66:67], 0
	v_mov_b64_e32 v[68:69], 0
	v_mov_b64_e32 v[70:71], 0
	v_mov_b64_e32 v[96:97], 0
	v_mov_b64_e32 v[98:99], 0
	v_mov_b64_e32 v[100:101], 0
	v_mov_b64_e32 v[102:103], 0
	v_mov_b64_e32 v[112:113], 0
	v_mov_b32_e32 v114, 0
	v_mov_b64_e32 v[72:73], 0
	v_mov_b64_e32 v[74:75], 0
	v_mov_b64_e32 v[76:77], 0
	v_mov_b64_e32 v[78:79], 0
	v_mov_b64_e32 v[104:105], 0
	v_mov_b64_e32 v[106:107], 0
	v_mov_b64_e32 v[108:109], 0
	v_mov_b64_e32 v[110:111], 0
	v_mov_b32_e32 v115, 0
	v_mov_b64_e32 v[116:117], 0
	v_mov_b64_e32 v[118:119], 0
	v_mov_b64_e32 v[120:121], 0
	v_mov_b64_e32 v[122:123], 0
	v_mov_b64_e32 v[124:125], 0
	v_mov_b64_e32 v[126:127], 0
	v_mov_b64_e32 v[128:129], 0
	v_mov_b64_e32 v[130:131], 0
	v_mov_b64_e32 v[132:133], 0
	v_mov_b64_e32 v[134:135], 0
	v_mov_b64_e32 v[136:137], 0
	v_mov_b64_e32 v[138:139], 0
	v_mov_b64_e32 v[140:141], 0
	v_mov_b64_e32 v[142:143], 0
